# m4 + converter workgroups (bid>=64) arrive at the grid barrier before the scan/conversion phase without waiting (they read only kernel inputs there)
# speedup vs baseline: 1.0147x; 1.0033x over previous
; __device__ __forceinline__ unsigned xb_ld(unsigned* p)              { return __hip_atomic_load(p, __ATOMIC_RELAXED, __HIP_MEMORY_SCOPE_AGENT); }
; __device__ __forceinline__ unsigned xb_add(unsigned* p, unsigned v) { return __hip_atomic_fetch_add(p, v, __ATOMIC_RELAXED, __HIP_MEMORY_SCOPE_AGENT); }
; #define XB_SPIN(cond, bar) do { unsigned _sp = 0; while (cond) { __builtin_amdgcn_s_sleep(1); \
;     if ((++_sp & 255u) == 0u) { if (xb_ld(&(bar)[XB_TMO])) break; if (_sp > XB_SPIN_CAP) { atomicAdd(&(bar)[XB_TMO], 1u); break; } } } } while (0)
; __device__ __forceinline__ void xcd_barrier(const XcdBarrier& b, const int wave) {
;     ...
;         unsigned nloc = b.st[0], nx = b.st[1];
;         if (nloc == 0u) { xcd_barrier_complete(bar, b.x, nloc, nx); b.st[0] = nloc; b.st[1] = nx; }
;         const unsigned old = xb_add(&bar[XB_XSUB(b.x)], 1u);
;         const unsigned gen = old / nloc;
;         if (old + 1u == (gen + 1u) * nloc) {
;             __builtin_amdgcn_fence(__ATOMIC_RELEASE, "agent");
;             asm volatile("s_waitcnt vmcnt(0)" ::: "memory");
;             const unsigned og = xb_add(&bar[XB_TOP], 1u);
;             const unsigned tg = og / nx;
;             if (og + 1u == (tg + 1u) * nx) xb_add(&bar[XB_TOPGEN], 1u);
;             else XB_SPIN(xb_ld(&bar[XB_TOPGEN]) == tg, bar);
;             __builtin_amdgcn_fence(__ATOMIC_ACQUIRE, "agent");
;             xb_add(&bar[XB_XGEN(b.x)], 1u);
;             asm volatile("s_waitcnt vmcnt(0)" ::: "memory");
;         } else {
;             XB_SPIN(xb_ld(&bar[XB_XGEN(b.x)]) == gen, bar);
.LBB0_729:
	s_or_b64 exec, exec, s[8:9]
	v_cvt_f32_u32_e32 v4, v2
	s_waitcnt vmcnt(0)
	v_readfirstlane_b32 s2, v3
	v_sub_u32_e32 v3, 0, v2
	v_rcp_iflag_f32_e32 v4, v4
	v_add_u32_e32 v5, s2, v1
	v_mul_f32_e32 v4, 0x4f7ffffe, v4
	v_cvt_u32_f32_e32 v4, v4
	v_mul_lo_u32 v1, v3, v4
	v_mul_hi_u32 v1, v4, v1
	v_add_u32_e32 v1, v4, v1
	v_mul_hi_u32 v1, v5, v1
	v_mul_lo_u32 v3, v1, v2
	v_sub_u32_e32 v3, v5, v3
	v_add_u32_e32 v4, 1, v1
	v_cmp_ge_u32_e32 vcc, v3, v2
	s_nop 1
	v_cndmask_b32_e32 v1, v1, v4, vcc
	v_sub_u32_e32 v4, v3, v2
	v_cndmask_b32_e32 v3, v3, v4, vcc
	v_add_u32_e32 v4, 1, v1
	v_cmp_ge_u32_e32 vcc, v3, v2
	v_add_u32_e32 v3, 1, v5
	s_nop 0
	v_cndmask_b32_e32 v1, v1, v4, vcc
	v_mul_lo_u32 v4, v2, v1
	v_add_u32_e32 v2, v4, v2
	v_cmp_ne_u32_e32 vcc, v3, v2
	s_and_saveexec_b64 s[2:3], vcc
	s_xor_b64 s[6:7], exec, s[2:3]
	s_cbranch_execz .LBB0_743
	s_waitcnt lgkmcnt(0)
	v_readlane_b32 s10, v254, 3
	s_cmp_gt_u32 s10, 63
	s_cbranch_scc1 .LBB0_763
	v_readlane_b32 s10, v254, 36
	v_readlane_b32 s11, v254, 37
	v_mov_b32_e32 v0, 0
	s_add_u32 s10, s10, 0x3500
	s_addc_u32 s11, s11, 0
	global_load_dword v0, v0, s[10:11] sc1
	s_waitcnt vmcnt(0)
	v_cmp_eq_u32_e32 vcc, v0, v1
	s_and_saveexec_b64 s[8:9], vcc
	s_cbranch_execz .LBB0_742
	s_mov_b32 s2, 1
	s_mov_b64 s[12:13], 0
	v_mov_b32_e32 v0, 0
	s_branch .LBB0_733

; __device__ __forceinline__ unsigned xb_ld(unsigned* p)              { return __hip_atomic_load(p, __ATOMIC_RELAXED, __HIP_MEMORY_SCOPE_AGENT); }
; __device__ __forceinline__ unsigned xb_add(unsigned* p, unsigned v) { return __hip_atomic_fetch_add(p, v, __ATOMIC_RELAXED, __HIP_MEMORY_SCOPE_AGENT); }
; #define XB_SPIN(cond, bar) do { unsigned _sp = 0; while (cond) { __builtin_amdgcn_s_sleep(1); \
;     if ((++_sp & 255u) == 0u) { if (xb_ld(&(bar)[XB_TMO])) break; if (_sp > XB_SPIN_CAP) { atomicAdd(&(bar)[XB_TMO], 1u); break; } } } } while (0)
; __device__ __forceinline__ void xcd_barrier(const XcdBarrier& b, const int wave) {
;     ...
;         unsigned nloc = b.st[0], nx = b.st[1];
;         if (nloc == 0u) { xcd_barrier_complete(bar, b.x, nloc, nx); b.st[0] = nloc; b.st[1] = nx; }
;         const unsigned old = xb_add(&bar[XB_XSUB(b.x)], 1u);
;         const unsigned gen = old / nloc;
;         if (old + 1u == (gen + 1u) * nloc) {
;             __builtin_amdgcn_fence(__ATOMIC_RELEASE, "agent");
;             asm volatile("s_waitcnt vmcnt(0)" ::: "memory");
;             const unsigned og = xb_add(&bar[XB_TOP], 1u);
;             const unsigned tg = og / nx;
;             if (og + 1u == (tg + 1u) * nx) xb_add(&bar[XB_TOPGEN], 1u);
;             else XB_SPIN(xb_ld(&bar[XB_TOPGEN]) == tg, bar);
;             __builtin_amdgcn_fence(__ATOMIC_ACQUIRE, "agent");
;             xb_add(&bar[XB_XGEN(b.x)], 1u);
;             asm volatile("s_waitcnt vmcnt(0)" ::: "memory");
;         } else {
;             XB_SPIN(xb_ld(&bar[XB_XGEN(b.x)]) == gen, bar);
.LBB0_746:
	s_or_b64 exec, exec, s[8:9]
	v_cvt_f32_u32_e32 v3, v0
	s_waitcnt vmcnt(0)
	v_readfirstlane_b32 s2, v2
	v_readlane_b32 s8, v254, 22
	v_readlane_b32 s22, v254, 36
	v_rcp_iflag_f32_e32 v3, v3
	v_add_u32_e32 v1, s2, v1
	v_add_u32_e32 v4, 1, v1
	v_readlane_b32 s9, v254, 23
	v_mul_f32_e32 v2, 0x4f7ffffe, v3
	v_cvt_u32_f32_e32 v2, v2
	v_sub_u32_e32 v3, 0, v0
	v_readlane_b32 s23, v254, 37
	s_add_u32 s8, s22, 0x3500
	v_mul_lo_u32 v3, v3, v2
	v_mul_hi_u32 v3, v2, v3
	v_add_u32_e32 v2, v2, v3
	v_mul_hi_u32 v2, v1, v2
	v_mul_lo_u32 v3, v2, v0
	v_sub_u32_e32 v1, v1, v3
	v_add_u32_e32 v5, 1, v2
	v_cmp_ge_u32_e32 vcc, v1, v0
	v_sub_u32_e32 v3, v1, v0
	v_readlane_b32 s10, v254, 24
	v_cndmask_b32_e32 v2, v2, v5, vcc
	v_cndmask_b32_e32 v1, v1, v3, vcc
	v_add_u32_e32 v3, 1, v2
	v_cmp_ge_u32_e32 vcc, v1, v0
	v_readlane_b32 s11, v254, 25
	s_addc_u32 s9, s23, 0
	v_cndmask_b32_e32 v2, v2, v3, vcc
	v_mul_lo_u32 v1, v0, v2
	v_add_u32_e32 v0, v1, v0
	v_cmp_ne_u32_e32 vcc, v4, v0
	s_mov_b64 s[10:11], -1
	v_mov_b64_e32 v[0:1], s[8:9]
	v_readlane_b32 s12, v254, 26
	v_readlane_b32 s13, v254, 27
	v_readlane_b32 s14, v254, 28
	v_readlane_b32 s15, v254, 29
	v_readlane_b32 s16, v254, 30
	v_readlane_b32 s17, v254, 31
	v_readlane_b32 s18, v254, 32
	v_readlane_b32 s19, v254, 33
	v_readlane_b32 s20, v254, 34
	v_readlane_b32 s21, v254, 35
	s_and_saveexec_b64 s[6:7], vcc
	s_cbranch_execz .LBB0_758
	v_readlane_b32 s14, v254, 3
	s_cmp_gt_u32 s14, 63
	s_cbranch_scc1 .LBB0_763
	v_mov_b32_e32 v0, 0
	global_load_dword v1, v0, s[8:9] sc1
	s_mov_b64 s[14:15], 0
	s_waitcnt vmcnt(0)
	v_cmp_eq_u32_e32 vcc, v1, v2
	s_and_saveexec_b64 s[12:13], vcc
	s_cbranch_execz .LBB0_757
	v_readlane_b32 s16, v254, 22
	v_readlane_b32 s30, v254, 36
	v_readlane_b32 s31, v254, 37
	s_add_u32 s10, s30, 0x200
	s_addc_u32 s11, s31, 0
	s_mov_b32 s2, 1
	v_readlane_b32 s17, v254, 23
	v_readlane_b32 s18, v254, 24
	v_readlane_b32 s19, v254, 25
	v_readlane_b32 s20, v254, 26
	v_readlane_b32 s21, v254, 27
	v_readlane_b32 s22, v254, 28
	v_readlane_b32 s23, v254, 29
	v_readlane_b32 s24, v254, 30
	v_readlane_b32 s25, v254, 31
	v_readlane_b32 s26, v254, 32
	v_readlane_b32 s27, v254, 33
	v_readlane_b32 s28, v254, 34
	v_readlane_b32 s29, v254, 35
	s_branch .LBB0_750
